# rwkv state scan: the Y stage (4 MFMAs + y store) moved from waves 0-3 to waves 4-7, which idle between the third barrier and the next chunk; waves 0-3 keep the state update and image writes
# speedup vs baseline: 1.0080x; 1.0060x over previous
; __device__ __forceinline__ unsigned cvt_pk_bf16(float lo, float hi) { const f32x2 v = {lo, hi}; const bf16x2_t b = __builtin_convertvector(v, bf16x2_t); return __builtin_bit_cast(unsigned, b); }
; #define ZERO4() ((f32x4){opaque0(), 0.f, 0.f, 0.f} * 0.f)
; __device__ __forceinline__ void rwkv_state_phase(LAS unsigned char* lds, const unsigned char* img, bf16_t* y_, const RwScan& a_, const int vcu, const int G, const int tid0_) {
;     ...
;             if (wave < 4) {
;                 const int mt = wave >> 1, nt = wave & 1;
;                 f32x4 y = ZERO4();
; #pragma unroll
;                 for (int ks = 0; ks < 2; ++ks) y = __builtin_amdgcn_mfma_f32_16x16x32_bf16(ldfrag(S0, P64, 16 * mt + fr, 32 * ks + 8 * fq), ldfrag(RT, P64, 16 * nt + fr, 32 * ks + 8 * fq), y, 0, 0, 0);
;                 y = __builtin_amdgcn_mfma_f32_16x16x32_bf16(ldfrag(Ui, P32, 16 * mt + fr, 8 * fq), ldfrag(MbrT, P32, 16 * nt + fr, 8 * fq), y, 0, 0, 0);
;                 y = __builtin_amdgcn_mfma_f32_16x16x32_bf16(ldfrag(Vi, P32, 16 * mt + fr, 8 * fq), ldfrag(MkrT, P32, 16 * nt + fr, 8 * fq), y, 0, 0, 0);
;                 u32x2 o; o.x = cvt_pk_bf16(y[0], y[1]); o.y = cvt_pk_bf16(y[2], y[3]);
;                 *(u32x2*)(y_ + (size_t)(b * SEQ + t0 + 16 * nt + fr) * 1024 + h * 64 + half * 32 + 16 * mt + 4 * fq) = o;
;             }
.LBB0_802:
	s_mov_b64 s[34:35], -1
	s_andn2_b64 vcc, exec, s[10:11]
	v_mul_u32_u24_e32 v101, 40, v95
	s_waitcnt lgkmcnt(0)
	s_barrier
	s_cbranch_vccnz .LBB0_804
	v_lshlrev_b32_e32 v5, 3, v96
	v_mul_lo_u32 v2, v100, 40
	v_mul_u32_u24_e32 v4, 40, v95
	s_mov_b64 s[34:35], 0
.LBB0_804:
	s_andn2_b64 vcc, exec, s[34:35]
	s_cbranch_vccnz .LBB0_746
	v_or_b32_e32 v118, s55, v81
	v_mul_lo_u32 v96, v118, s67
	v_mov_b32_e32 v2, v3
	v_add3_u32 v96, s65, v96, v99
	v_mul_lo_u32 v114, v118, 40
	v_lshlrev_b32_e32 v116, 6, v95
	v_lshlrev_b32_e32 v117, 6, v118
	v_lshlrev_b32_e32 v115, 1, v114
	v_sub_u32_e32 v116, v98, v116
	v_sub_u32_e32 v117, v96, v117
	v_add3_u32 v115, 0, v115, v99
	ds_read_b128 v[102:105], v96 offset:9216
	ds_read_b128 v[106:109], v98 offset:4608
	ds_read_b128 v[160:163], v96 offset:9280
	ds_read_b128 v[164:167], v98 offset:4672
	ds_read_b128 v[168:171], v115 offset:29184
	ds_read_b128 v[172:175], v116 offset:16384
	ds_read_b128 v[176:179], v117 offset:24064
	ds_read_b128 v[180:183], v116 offset:18944
	v_mul_f32_e32 v2, 0, v2
	v_mov_b32_e32 v4, v3
	v_mov_b32_e32 v5, v3
	s_waitcnt lgkmcnt(6)
	s_nop 0
	v_mfma_f32_16x16x32_bf16 v[102:105], v[102:105], v[106:109], v[2:5]
	v_add_u32_e32 v98, s33, v81
	v_ashrrev_i32_e32 v99, 31, v98
	s_waitcnt lgkmcnt(4)
	v_mfma_f32_16x16x32_bf16 v[102:105], v[160:163], v[164:167], v[102:105]
	s_waitcnt lgkmcnt(2)
	v_mfma_f32_16x16x32_bf16 v[102:105], v[168:171], v[172:175], v[102:105]
	v_mul_lo_u32 v2, v100, 40
	s_waitcnt lgkmcnt(0)
	v_mfma_f32_16x16x32_bf16 v[102:105], v[176:179], v[180:183], v[102:105]
	v_lshlrev_b64 v[98:99], 11, v[98:99]
	v_lshl_add_u64 v[98:99], s[2:3], 0, v[98:99]
	v_mov_b32_e32 v95, v3
	s_nop 4
	v_cvt_pk_bf16_f32 v4, v102, v103
	v_cvt_pk_bf16_f32 v5, v104, v105
	v_lshl_add_u64 v[94:95], v[98:99], 0, v[94:95]
	global_store_dwordx2 v[94:95], v[4:5], off offset:-64
	v_mov_b32_e32 v4, v101
	v_mov_b32_e32 v5, v79
	s_branch .LBB0_746
